# expert-down GEMM epilogue: eight gate loads issued together with counted waits (was load-wait-store ladder); on top of v22
# speedup vs baseline: 1.0262x; 1.0037x over previous
; __device__ __forceinline__ unsigned pk2(float lo, float hi) { return f2bf(lo) | (f2bf(hi) << 16); }
;     __device__ __forceinline__ void epi(const f32x4 (&acc)[2][2][4][2], const Unit& u, int wr, int wc, int fr, int fq) const {
;         const int e = u.pm / tpe, t = u.pm - e * tpe; const size_t rowt = (size_t)e * EROWS + (size_t)t * 256;
;         char* base = (char*)(YE + rowt * 2048 + (size_t)u.pn * 256); const char* gp = (const char*)(gatev + rowt);
;         unsigned loff = (unsigned)((wr * 64 + fr) * 2048 + wc * 32 + 8 * fq) * 2u, goff = (unsigned)(wr * 64 + fr) * 4u; asm volatile("" : "+v"(loff), "+v"(goff));
; #pragma unroll
;         for (int ai = 0; ai < 2; ++ai)
; #pragma unroll
;             for (int m = 0; m < 4; ++m) { const float g = *(const float*)(gp + (ai * 128 + m * 16) * 4 + goff) * (1.f / W8_SCALE);
; #pragma unroll
;                 for (int bj = 0; bj < 2; ++bj) { const f32x4 v0 = acc[ai][bj][m][0] * g, v1 = acc[ai][bj][m][1] * g;
;                     u32x4 w; w.x = pk2(v0[0], v0[1]); w.y = pk2(v0[2], v0[3]); w.z = pk2(v1[0], v1[1]); w.w = pk2(v1[2], v1[3]);
;                     *(u32x4*)(base + ((size_t)(ai * 128 + m * 16) * 2048 + bj * 128) * 2 + loff) = w; } }
.LBB0_2666:
	s_abs_i32 s18, s17
	s_mul_hi_u32 s19, s18, s45
	s_mul_i32 s20, s19, s24
	s_sub_i32 s18, s18, s20
	s_ashr_i32 s11, s17, 31
	s_add_i32 s20, s19, 1
	s_sub_i32 s21, s18, s24
	s_cmp_ge_u32 s18, s24
	s_cselect_b32 s19, s20, s19
	s_cselect_b32 s18, s21, s18
	s_add_i32 s20, s19, 1
	s_cmp_ge_u32 s18, s24
	s_cselect_b32 s18, s20, s19
	s_xor_b32 s18, s18, s11
	s_sub_i32 s11, s18, s11
	s_mul_i32 s18, s11, s24
	s_sub_i32 s18, s17, s18
	s_ashr_i32 s19, s18, 31
	s_mul_hi_i32 s17, s11, 0x900
	s_mulk_i32 s11, 0x900
	s_lshl_b64 s[18:19], s[18:19], 8
	s_add_u32 s20, s18, s11
	s_addc_u32 s21, s19, s17
	s_lshl_b64 s[18:19], s[20:21], 12
	s_add_u32 s11, s50, s18
	s_addc_u32 s19, s51, s19
	s_ashr_i32 s17, s16, 31
	s_lshl_b64 s[16:17], s[16:17], 9
	s_add_u32 s18, s11, s16
	s_addc_u32 s19, s19, s17
	s_lshl_b64 s[16:17], s[20:21], 2
	s_add_u32 s16, s52, s16
	s_addc_u32 s17, s53, s17
	v_mov_b32_e32 v4, v186
	v_mov_b32_e32 v146, v188
	global_load_dword v1, v4, s[16:17]
	global_load_dword v176, v4, s[16:17] offset:64
	global_load_dword v177, v4, s[16:17] offset:128
	global_load_dword v178, v4, s[16:17] offset:192
	global_load_dword v179, v4, s[16:17] offset:512
	global_load_dword v182, v4, s[16:17] offset:576
	global_load_dword v183, v4, s[16:17] offset:640
	global_load_dword v184, v4, s[16:17] offset:704
	s_mov_b32 s11, 0x20000
	s_waitcnt vmcnt(7)
	v_mul_f32_e32 v2, 0x3c800000, v1
	v_pk_mul_f32 v[6:7], v[162:163], v[2:3] op_sel_hi:[1,0]
	v_pk_mul_f32 v[8:9], v[160:161], v[2:3] op_sel_hi:[1,0]
	v_pk_mul_f32 v[10:11], v[158:159], v[2:3] op_sel_hi:[1,0]
	v_pk_mul_f32 v[12:13], v[156:157], v[2:3] op_sel_hi:[1,0]
	v_pk_mul_f32 v[14:15], v[154:155], v[2:3] op_sel_hi:[1,0]
	v_pk_mul_f32 v[16:17], v[152:153], v[2:3] op_sel_hi:[1,0]
	v_pk_mul_f32 v[18:19], v[150:151], v[2:3] op_sel_hi:[1,0]
	v_pk_mul_f32 v[2:3], v[148:149], v[2:3] op_sel_hi:[1,0]
	v_bfe_u32 v1, v8, 16, 1
	v_bfe_u32 v20, v6, 16, 1
	v_bfe_u32 v22, v12, 16, 1
	v_bfe_u32 v24, v10, 16, 1
	v_bfe_u32 v5, v9, 16, 1
	v_bfe_u32 v21, v7, 16, 1
	v_bfe_u32 v23, v13, 16, 1
	v_bfe_u32 v25, v11, 16, 1
	v_bfe_u32 v26, v16, 16, 1
	v_bfe_u32 v28, v14, 16, 1
	v_bfe_u32 v30, v2, 16, 1
	v_bfe_u32 v32, v18, 16, 1
	v_add3_u32 v1, v8, v1, s37
	v_add3_u32 v6, v6, v20, s37
	v_add3_u32 v8, v12, v22, s37
	v_add3_u32 v10, v10, v24, s37
	v_bfe_u32 v27, v17, 16, 1
	v_bfe_u32 v29, v15, 16, 1
	v_bfe_u32 v31, v3, 16, 1
	v_bfe_u32 v33, v19, 16, 1
	v_add3_u32 v5, v9, v5, s37
	v_add3_u32 v7, v7, v21, s37
	v_add3_u32 v9, v13, v23, s37
	v_add3_u32 v11, v11, v25, s37
	v_add3_u32 v12, v16, v26, s37
	v_add3_u32 v14, v14, v28, s37
	v_add3_u32 v2, v2, v30, s37
	v_add3_u32 v16, v18, v32, s37
	v_lshrrev_b32_e32 v1, 16, v1
	v_lshrrev_b32_e32 v18, 16, v6
	v_lshrrev_b32_e32 v8, 16, v8
	v_lshrrev_b32_e32 v10, 16, v10
	v_add3_u32 v13, v17, v27, s37
	v_add3_u32 v15, v15, v29, s37
	v_add3_u32 v3, v3, v31, s37
	v_add3_u32 v17, v19, v33, s37
	v_lshrrev_b32_e32 v12, 16, v12
	v_lshrrev_b32_e32 v14, 16, v14
	v_lshrrev_b32_e32 v2, 16, v2
	v_lshrrev_b32_e32 v16, 16, v16
	v_and_or_b32 v6, v5, s33, v1
	v_and_or_b32 v7, v7, s33, v18
	v_and_or_b32 v8, v9, s33, v8
	v_and_or_b32 v9, v11, s33, v10
	v_and_or_b32 v10, v13, s33, v12
	v_and_or_b32 v11, v15, s33, v14
	v_and_or_b32 v12, v3, s33, v2
	v_and_or_b32 v13, v17, s33, v16
	global_store_dwordx4 v146, v[6:9], s[18:19]
	global_store_dwordx4 v146, v[10:13], s[18:19] offset:256
	s_nop 0
	v_lshl_add_u64 v[2:3], s[18:19], 0, v[146:147]
	v_add_co_u32_e32 v14, vcc, s81, v2
	s_waitcnt vmcnt(8)
	v_mul_f32_e32 v6, 0x3c800000, v176
	v_pk_mul_f32 v[8:9], v[144:145], v[6:7] op_sel_hi:[1,0]
	v_pk_mul_f32 v[10:11], v[142:143], v[6:7] op_sel_hi:[1,0]
	v_pk_mul_f32 v[12:13], v[140:141], v[6:7] op_sel_hi:[1,0]
	v_pk_mul_f32 v[16:17], v[138:139], v[6:7] op_sel_hi:[1,0]
	v_pk_mul_f32 v[18:19], v[136:137], v[6:7] op_sel_hi:[1,0]
	v_pk_mul_f32 v[20:21], v[134:135], v[6:7] op_sel_hi:[1,0]
	v_pk_mul_f32 v[22:23], v[132:133], v[6:7] op_sel_hi:[1,0]
	v_pk_mul_f32 v[6:7], v[130:131], v[6:7] op_sel_hi:[1,0]
	v_bfe_u32 v1, v10, 16, 1
	v_bfe_u32 v24, v8, 16, 1
	v_bfe_u32 v26, v16, 16, 1
	v_bfe_u32 v28, v12, 16, 1
	v_bfe_u32 v5, v11, 16, 1
	v_bfe_u32 v25, v9, 16, 1
	v_bfe_u32 v27, v17, 16, 1
	v_bfe_u32 v29, v13, 16, 1
	v_bfe_u32 v30, v20, 16, 1
	v_bfe_u32 v32, v18, 16, 1
	v_bfe_u32 v130, v6, 16, 1
	v_bfe_u32 v131, v7, 16, 1
	v_bfe_u32 v132, v22, 16, 1
	v_add3_u32 v1, v10, v1, s37
	v_add3_u32 v8, v8, v24, s37
	v_add3_u32 v10, v16, v26, s37
	v_add3_u32 v12, v12, v28, s37
	v_bfe_u32 v31, v21, 16, 1
	v_bfe_u32 v33, v19, 16, 1
	v_bfe_u32 v133, v23, 16, 1
	v_add3_u32 v5, v11, v5, s37
	v_add3_u32 v9, v9, v25, s37
	v_add3_u32 v11, v17, v27, s37
	v_add3_u32 v13, v13, v29, s37
	v_add3_u32 v16, v20, v30, s37
	v_add3_u32 v18, v18, v32, s37
	v_add3_u32 v6, v6, v130, s37
	v_add3_u32 v20, v7, v131, s37
	v_add3_u32 v7, v22, v132, s37
	v_lshrrev_b32_e32 v1, 16, v1
	v_lshrrev_b32_e32 v8, 16, v8
	v_lshrrev_b32_e32 v10, 16, v10
	v_lshrrev_b32_e32 v12, 16, v12
	v_addc_co_u32_e32 v15, vcc, 0, v3, vcc
	v_add3_u32 v17, v21, v31, s37
	v_add3_u32 v19, v19, v33, s37
	v_add3_u32 v21, v23, v133, s37
	v_lshrrev_b32_e32 v16, 16, v16
	v_lshrrev_b32_e32 v18, 16, v18
	v_lshrrev_b32_e32 v22, 16, v6
	v_lshrrev_b32_e32 v23, 16, v7
	v_and_or_b32 v6, v5, s33, v1
	v_and_or_b32 v7, v9, s33, v8
	v_and_or_b32 v8, v11, s33, v10
	v_and_or_b32 v9, v13, s33, v12
	v_and_or_b32 v10, v17, s33, v16
	v_and_or_b32 v11, v19, s33, v18
	v_and_or_b32 v12, v20, s33, v22
	v_and_or_b32 v13, v21, s33, v23
	global_store_dwordx4 v[14:15], v[6:9], off
	global_store_dwordx4 v[14:15], v[10:13], off offset:256
	s_nop 0
	v_add_co_u32_e32 v14, vcc, s11, v2
	s_mov_b32 s11, 0x30000
	s_nop 0
	v_addc_co_u32_e32 v15, vcc, 0, v3, vcc
	s_waitcnt vmcnt(9)
; __device__ __forceinline__ unsigned pk2(float lo, float hi) { return f2bf(lo) | (f2bf(hi) << 16); }
;     __device__ __forceinline__ void epi(const f32x4 (&acc)[2][2][4][2], const Unit& u, int wr, int wc, int fr, int fq) const {
;     ...
;             for (int m = 0; m < 4; ++m) { const float g = *(const float*)(gp + (ai * 128 + m * 16) * 4 + goff) * (1.f / W8_SCALE);
; #pragma unroll
;                 for (int bj = 0; bj < 2; ++bj) { const f32x4 v0 = acc[ai][bj][m][0] * g, v1 = acc[ai][bj][m][1] * g;
;                     u32x4 w; w.x = pk2(v0[0], v0[1]); w.y = pk2(v0[2], v0[3]); w.z = pk2(v1[0], v1[1]); w.w = pk2(v1[2], v1[3]);
;                     *(u32x4*)(base + ((size_t)(ai * 128 + m * 16) * 2048 + bj * 128) * 2 + loff) = w; } }
	v_mul_f32_e32 v6, 0x3c800000, v177
	v_pk_mul_f32 v[8:9], v[128:129], v[6:7] op_sel_hi:[1,0]
	v_pk_mul_f32 v[10:11], v[126:127], v[6:7] op_sel_hi:[1,0]
	v_pk_mul_f32 v[12:13], v[124:125], v[6:7] op_sel_hi:[1,0]
	v_pk_mul_f32 v[16:17], v[122:123], v[6:7] op_sel_hi:[1,0]
	v_pk_mul_f32 v[18:19], v[120:121], v[6:7] op_sel_hi:[1,0]
	v_pk_mul_f32 v[20:21], v[118:119], v[6:7] op_sel_hi:[1,0]
	v_pk_mul_f32 v[22:23], v[116:117], v[6:7] op_sel_hi:[1,0]
	v_pk_mul_f32 v[6:7], v[114:115], v[6:7] op_sel_hi:[1,0]
	v_bfe_u32 v1, v10, 16, 1
	v_bfe_u32 v24, v8, 16, 1
	v_bfe_u32 v26, v16, 16, 1
	v_bfe_u32 v28, v12, 16, 1
	v_bfe_u32 v5, v11, 16, 1
	v_bfe_u32 v25, v9, 16, 1
	v_bfe_u32 v27, v17, 16, 1
	v_bfe_u32 v29, v13, 16, 1
	v_bfe_u32 v30, v20, 16, 1
	v_bfe_u32 v32, v18, 16, 1
	v_bfe_u32 v114, v6, 16, 1
	v_bfe_u32 v115, v7, 16, 1
	v_bfe_u32 v116, v22, 16, 1
	v_add3_u32 v1, v10, v1, s37
	v_add3_u32 v8, v8, v24, s37
	v_add3_u32 v10, v16, v26, s37
	v_add3_u32 v12, v12, v28, s37
	v_bfe_u32 v31, v21, 16, 1
	v_bfe_u32 v33, v19, 16, 1
	v_bfe_u32 v117, v23, 16, 1
	v_add3_u32 v5, v11, v5, s37
	v_add3_u32 v9, v9, v25, s37
	v_add3_u32 v11, v17, v27, s37
	v_add3_u32 v13, v13, v29, s37
	v_add3_u32 v16, v20, v30, s37
	v_add3_u32 v18, v18, v32, s37
	v_add3_u32 v6, v6, v114, s37
	v_add3_u32 v20, v7, v115, s37
	v_add3_u32 v7, v22, v116, s37
	v_lshrrev_b32_e32 v1, 16, v1
	v_lshrrev_b32_e32 v8, 16, v8
	v_lshrrev_b32_e32 v10, 16, v10
	v_lshrrev_b32_e32 v12, 16, v12
	v_add3_u32 v17, v21, v31, s37
	v_add3_u32 v19, v19, v33, s37
	v_add3_u32 v21, v23, v117, s37
	v_lshrrev_b32_e32 v16, 16, v16
	v_lshrrev_b32_e32 v18, 16, v18
	v_lshrrev_b32_e32 v22, 16, v6
	v_lshrrev_b32_e32 v23, 16, v7
	v_and_or_b32 v6, v5, s33, v1
	v_and_or_b32 v7, v9, s33, v8
	v_and_or_b32 v8, v11, s33, v10
	v_and_or_b32 v9, v13, s33, v12
	v_and_or_b32 v10, v17, s33, v16
	v_and_or_b32 v11, v19, s33, v18
	v_and_or_b32 v12, v20, s33, v22
	v_and_or_b32 v13, v21, s33, v23
	global_store_dwordx4 v[14:15], v[6:9], off
	global_store_dwordx4 v[14:15], v[10:13], off offset:256
	s_nop 0
	v_add_co_u32_e32 v14, vcc, s11, v2
	s_mov_b32 s11, 0x80000
	s_nop 0
	v_addc_co_u32_e32 v15, vcc, 0, v3, vcc
	s_waitcnt vmcnt(10)
	v_mul_f32_e32 v6, 0x3c800000, v178
	v_pk_mul_f32 v[8:9], v[112:113], v[6:7] op_sel_hi:[1,0]
	v_pk_mul_f32 v[10:11], v[110:111], v[6:7] op_sel_hi:[1,0]
	v_pk_mul_f32 v[12:13], v[108:109], v[6:7] op_sel_hi:[1,0]
	v_pk_mul_f32 v[16:17], v[106:107], v[6:7] op_sel_hi:[1,0]
	v_pk_mul_f32 v[18:19], v[104:105], v[6:7] op_sel_hi:[1,0]
	v_pk_mul_f32 v[20:21], v[102:103], v[6:7] op_sel_hi:[1,0]
	v_pk_mul_f32 v[22:23], v[100:101], v[6:7] op_sel_hi:[1,0]
	v_pk_mul_f32 v[6:7], v[98:99], v[6:7] op_sel_hi:[1,0]
	v_bfe_u32 v1, v10, 16, 1
	v_bfe_u32 v24, v8, 16, 1
	v_bfe_u32 v26, v16, 16, 1
	v_bfe_u32 v28, v12, 16, 1
	v_bfe_u32 v5, v11, 16, 1
	v_bfe_u32 v25, v9, 16, 1
	v_bfe_u32 v27, v17, 16, 1
	v_bfe_u32 v29, v13, 16, 1
	v_bfe_u32 v30, v20, 16, 1
	v_bfe_u32 v32, v18, 16, 1
	v_bfe_u32 v98, v6, 16, 1
	v_bfe_u32 v99, v7, 16, 1
	v_bfe_u32 v100, v22, 16, 1
	v_add3_u32 v1, v10, v1, s37
	v_add3_u32 v8, v8, v24, s37
	v_add3_u32 v10, v16, v26, s37
	v_add3_u32 v12, v12, v28, s37
	v_bfe_u32 v31, v21, 16, 1
	v_bfe_u32 v33, v19, 16, 1
	v_bfe_u32 v101, v23, 16, 1
	v_add3_u32 v5, v11, v5, s37
	v_add3_u32 v9, v9, v25, s37
	v_add3_u32 v11, v17, v27, s37
	v_add3_u32 v13, v13, v29, s37
	v_add3_u32 v16, v20, v30, s37
	v_add3_u32 v18, v18, v32, s37
	v_add3_u32 v6, v6, v98, s37
	v_add3_u32 v20, v7, v99, s37
	v_add3_u32 v7, v22, v100, s37
	v_lshrrev_b32_e32 v1, 16, v1
	v_lshrrev_b32_e32 v8, 16, v8
	v_lshrrev_b32_e32 v10, 16, v10
	v_lshrrev_b32_e32 v12, 16, v12
	v_add3_u32 v17, v21, v31, s37
	v_add3_u32 v19, v19, v33, s37
	v_add3_u32 v21, v23, v101, s37
	v_lshrrev_b32_e32 v16, 16, v16
	v_lshrrev_b32_e32 v18, 16, v18
	v_lshrrev_b32_e32 v22, 16, v6
	v_lshrrev_b32_e32 v23, 16, v7
	v_and_or_b32 v6, v5, s33, v1
	v_and_or_b32 v7, v9, s33, v8
	v_and_or_b32 v8, v11, s33, v10
	v_and_or_b32 v9, v13, s33, v12
	v_and_or_b32 v10, v17, s33, v16
	v_and_or_b32 v11, v19, s33, v18
	v_and_or_b32 v12, v20, s33, v22
	v_and_or_b32 v13, v21, s33, v23
	global_store_dwordx4 v[14:15], v[6:9], off
	global_store_dwordx4 v[14:15], v[10:13], off offset:256
	s_nop 0
	v_add_co_u32_e32 v14, vcc, s11, v2
	s_mov_b32 s11, 0x90000
	s_nop 0
	v_addc_co_u32_e32 v15, vcc, 0, v3, vcc
	s_waitcnt vmcnt(11)
	v_mul_f32_e32 v6, 0x3c800000, v179
	v_pk_mul_f32 v[8:9], v[96:97], v[6:7] op_sel_hi:[1,0]
	v_pk_mul_f32 v[10:11], v[94:95], v[6:7] op_sel_hi:[1,0]
	v_pk_mul_f32 v[12:13], v[92:93], v[6:7] op_sel_hi:[1,0]
	v_pk_mul_f32 v[16:17], v[90:91], v[6:7] op_sel_hi:[1,0]
	v_pk_mul_f32 v[18:19], v[88:89], v[6:7] op_sel_hi:[1,0]
	v_pk_mul_f32 v[20:21], v[86:87], v[6:7] op_sel_hi:[1,0]
	v_pk_mul_f32 v[22:23], v[84:85], v[6:7] op_sel_hi:[1,0]
	v_pk_mul_f32 v[6:7], v[82:83], v[6:7] op_sel_hi:[1,0]
	v_bfe_u32 v1, v10, 16, 1
	v_bfe_u32 v24, v8, 16, 1
	v_bfe_u32 v26, v16, 16, 1
	v_bfe_u32 v28, v12, 16, 1
	v_bfe_u32 v5, v11, 16, 1
	v_bfe_u32 v25, v9, 16, 1
	v_bfe_u32 v27, v17, 16, 1
	v_bfe_u32 v29, v13, 16, 1
	v_bfe_u32 v30, v20, 16, 1
	v_bfe_u32 v32, v18, 16, 1
	v_bfe_u32 v82, v6, 16, 1
	v_bfe_u32 v83, v7, 16, 1
	v_bfe_u32 v84, v22, 16, 1
	v_add3_u32 v1, v10, v1, s37
	v_add3_u32 v8, v8, v24, s37
	v_add3_u32 v10, v16, v26, s37
	v_add3_u32 v12, v12, v28, s37
	v_bfe_u32 v31, v21, 16, 1
	v_bfe_u32 v33, v19, 16, 1
	v_bfe_u32 v85, v23, 16, 1
	v_add3_u32 v5, v11, v5, s37
	v_add3_u32 v9, v9, v25, s37
	v_add3_u32 v11, v17, v27, s37
	v_add3_u32 v13, v13, v29, s37
	v_add3_u32 v16, v20, v30, s37
	v_add3_u32 v18, v18, v32, s37
	v_add3_u32 v6, v6, v82, s37
	v_add3_u32 v20, v7, v83, s37
	v_add3_u32 v7, v22, v84, s37
	v_lshrrev_b32_e32 v1, 16, v1
	v_lshrrev_b32_e32 v8, 16, v8
	v_lshrrev_b32_e32 v10, 16, v10
	v_lshrrev_b32_e32 v12, 16, v12
	v_add3_u32 v17, v21, v31, s37
	v_add3_u32 v19, v19, v33, s37
	v_add3_u32 v21, v23, v85, s37
	v_lshrrev_b32_e32 v16, 16, v16
	v_lshrrev_b32_e32 v18, 16, v18
	v_lshrrev_b32_e32 v22, 16, v6
	v_lshrrev_b32_e32 v23, 16, v7
	v_and_or_b32 v6, v5, s33, v1
	v_and_or_b32 v7, v9, s33, v8
	v_and_or_b32 v8, v11, s33, v10
	v_and_or_b32 v9, v13, s33, v12
	v_and_or_b32 v10, v17, s33, v16
	v_and_or_b32 v11, v19, s33, v18
	v_and_or_b32 v12, v20, s33, v22
	v_and_or_b32 v13, v21, s33, v23
	global_store_dwordx4 v[14:15], v[6:9], off
	global_store_dwordx4 v[14:15], v[10:13], off offset:256
	s_nop 0
	v_add_co_u32_e32 v14, vcc, s11, v2
	s_mov_b32 s11, 0xa0000
	s_nop 0
	v_addc_co_u32_e32 v15, vcc, 0, v3, vcc
	s_waitcnt vmcnt(12)
; __device__ __forceinline__ unsigned pk2(float lo, float hi) { return f2bf(lo) | (f2bf(hi) << 16); }
; #define PG8_BAR __builtin_amdgcn_s_barrier()
; template <class P>
; __device__ __forceinline__ void gemm_phase(LAS unsigned char* lds, const P& p) {
;     ...
;         if (!has_next) break;
; #pragma unroll
;         for (int a = 0; a < 2; ++a)
; #pragma unroll
;             for (int b = 0; b < 2; ++b)
; #pragma unroll
;                 for (int m = 0; m < 4; ++m)
; #pragma unroll
;                     for (int n = 0; n < 2; ++n) acc[a][b][m][n] = (f32x4){0.f, 0.f, 0.f, 0.f};
;         cur = nxt; cA = nA; cB = nB; ++ui;
;         if (wr == 1) PG8_BAR;
;     __device__ __forceinline__ void epi(const f32x4 (&acc)[2][2][4][2], const Unit& u, int wr, int wc, int fr, int fq) const {
;     ...
;             for (int m = 0; m < 4; ++m) { const float g = *(const float*)(gp + (ai * 128 + m * 16) * 4 + goff) * (1.f / W8_SCALE);
; #pragma unroll
;                 for (int bj = 0; bj < 2; ++bj) { const f32x4 v0 = acc[ai][bj][m][0] * g, v1 = acc[ai][bj][m][1] * g;
;                     u32x4 w; w.x = pk2(v0[0], v0[1]); w.y = pk2(v0[2], v0[3]); w.z = pk2(v1[0], v1[1]); w.w = pk2(v1[2], v1[3]);
;                     *(u32x4*)(base + ((size_t)(ai * 128 + m * 16) * 2048 + bj * 128) * 2 + loff) = w; } }
	v_mul_f32_e32 v6, 0x3c800000, v182
	v_pk_mul_f32 v[8:9], v[80:81], v[6:7] op_sel_hi:[1,0]
	v_pk_mul_f32 v[10:11], v[78:79], v[6:7] op_sel_hi:[1,0]
	v_pk_mul_f32 v[12:13], v[76:77], v[6:7] op_sel_hi:[1,0]
	v_pk_mul_f32 v[16:17], v[74:75], v[6:7] op_sel_hi:[1,0]
	v_pk_mul_f32 v[18:19], v[72:73], v[6:7] op_sel_hi:[1,0]
	v_pk_mul_f32 v[20:21], v[70:71], v[6:7] op_sel_hi:[1,0]
	v_pk_mul_f32 v[22:23], v[68:69], v[6:7] op_sel_hi:[1,0]
	v_pk_mul_f32 v[6:7], v[66:67], v[6:7] op_sel_hi:[1,0]
	v_bfe_u32 v1, v10, 16, 1
	v_bfe_u32 v24, v8, 16, 1
	v_bfe_u32 v26, v16, 16, 1
	v_bfe_u32 v28, v12, 16, 1
	v_bfe_u32 v5, v11, 16, 1
	v_bfe_u32 v25, v9, 16, 1
	v_bfe_u32 v27, v17, 16, 1
	v_bfe_u32 v29, v13, 16, 1
	v_bfe_u32 v30, v20, 16, 1
	v_bfe_u32 v32, v18, 16, 1
	v_bfe_u32 v66, v6, 16, 1
	v_bfe_u32 v67, v7, 16, 1
	v_bfe_u32 v68, v22, 16, 1
	v_add3_u32 v1, v10, v1, s37
	v_add3_u32 v8, v8, v24, s37
	v_add3_u32 v10, v16, v26, s37
	v_add3_u32 v12, v12, v28, s37
	v_bfe_u32 v31, v21, 16, 1
	v_bfe_u32 v33, v19, 16, 1
	v_bfe_u32 v69, v23, 16, 1
	v_add3_u32 v5, v11, v5, s37
	v_add3_u32 v9, v9, v25, s37
	v_add3_u32 v11, v17, v27, s37
	v_add3_u32 v13, v13, v29, s37
	v_add3_u32 v16, v20, v30, s37
	v_add3_u32 v18, v18, v32, s37
	v_add3_u32 v6, v6, v66, s37
	v_add3_u32 v20, v7, v67, s37
	v_add3_u32 v7, v22, v68, s37
	v_lshrrev_b32_e32 v1, 16, v1
	v_lshrrev_b32_e32 v8, 16, v8
	v_lshrrev_b32_e32 v10, 16, v10
	v_lshrrev_b32_e32 v12, 16, v12
	v_add3_u32 v17, v21, v31, s37
	v_add3_u32 v19, v19, v33, s37
	v_add3_u32 v21, v23, v69, s37
	v_lshrrev_b32_e32 v16, 16, v16
	v_lshrrev_b32_e32 v18, 16, v18
	v_lshrrev_b32_e32 v22, 16, v6
	v_lshrrev_b32_e32 v23, 16, v7
	v_and_or_b32 v6, v5, s33, v1
	v_and_or_b32 v7, v9, s33, v8
	v_and_or_b32 v8, v11, s33, v10
	v_and_or_b32 v9, v13, s33, v12
	v_and_or_b32 v10, v17, s33, v16
	v_and_or_b32 v11, v19, s33, v18
	v_and_or_b32 v12, v20, s33, v22
	v_and_or_b32 v13, v21, s33, v23
	global_store_dwordx4 v[14:15], v[6:9], off
	global_store_dwordx4 v[14:15], v[10:13], off offset:256
	s_nop 0
	v_add_co_u32_e32 v14, vcc, s11, v2
	s_mov_b32 s11, 0xb0000
	s_nop 0
	v_addc_co_u32_e32 v15, vcc, 0, v3, vcc
	s_waitcnt vmcnt(13)
	v_mul_f32_e32 v6, 0x3c800000, v183
	v_pk_mul_f32 v[8:9], v[64:65], v[6:7] op_sel_hi:[1,0]
	v_pk_mul_f32 v[10:11], v[62:63], v[6:7] op_sel_hi:[1,0]
	v_pk_mul_f32 v[12:13], v[60:61], v[6:7] op_sel_hi:[1,0]
	v_pk_mul_f32 v[16:17], v[58:59], v[6:7] op_sel_hi:[1,0]
	v_pk_mul_f32 v[18:19], v[56:57], v[6:7] op_sel_hi:[1,0]
	v_pk_mul_f32 v[20:21], v[54:55], v[6:7] op_sel_hi:[1,0]
	v_pk_mul_f32 v[22:23], v[52:53], v[6:7] op_sel_hi:[1,0]
	v_pk_mul_f32 v[6:7], v[50:51], v[6:7] op_sel_hi:[1,0]
	v_bfe_u32 v1, v10, 16, 1
	v_bfe_u32 v24, v8, 16, 1
	v_bfe_u32 v26, v16, 16, 1
	v_bfe_u32 v28, v12, 16, 1
	v_bfe_u32 v5, v11, 16, 1
	v_bfe_u32 v25, v9, 16, 1
	v_bfe_u32 v27, v17, 16, 1
	v_bfe_u32 v29, v13, 16, 1
	v_bfe_u32 v30, v20, 16, 1
	v_bfe_u32 v32, v18, 16, 1
	v_bfe_u32 v50, v6, 16, 1
	v_bfe_u32 v51, v7, 16, 1
	v_bfe_u32 v52, v22, 16, 1
	v_add3_u32 v1, v10, v1, s37
	v_add3_u32 v8, v8, v24, s37
	v_add3_u32 v10, v16, v26, s37
	v_add3_u32 v12, v12, v28, s37
	v_bfe_u32 v31, v21, 16, 1
	v_bfe_u32 v33, v19, 16, 1
	v_bfe_u32 v53, v23, 16, 1
	v_add3_u32 v5, v11, v5, s37
	v_add3_u32 v9, v9, v25, s37
	v_add3_u32 v11, v17, v27, s37
	v_add3_u32 v13, v13, v29, s37
	v_add3_u32 v16, v20, v30, s37
	v_add3_u32 v18, v18, v32, s37
	v_add3_u32 v6, v6, v50, s37
	v_add3_u32 v20, v7, v51, s37
	v_add3_u32 v7, v22, v52, s37
	v_lshrrev_b32_e32 v1, 16, v1
	v_lshrrev_b32_e32 v8, 16, v8
	v_lshrrev_b32_e32 v10, 16, v10
	v_lshrrev_b32_e32 v12, 16, v12
	v_add3_u32 v17, v21, v31, s37
	v_add3_u32 v19, v19, v33, s37
	v_add3_u32 v21, v23, v53, s37
	v_lshrrev_b32_e32 v16, 16, v16
	v_lshrrev_b32_e32 v18, 16, v18
	v_lshrrev_b32_e32 v22, 16, v6
	v_lshrrev_b32_e32 v23, 16, v7
	v_and_or_b32 v6, v5, s33, v1
	v_and_or_b32 v7, v9, s33, v8
	v_and_or_b32 v8, v11, s33, v10
	v_and_or_b32 v9, v13, s33, v12
	v_and_or_b32 v10, v17, s33, v16
	v_and_or_b32 v11, v19, s33, v18
	v_and_or_b32 v12, v20, s33, v22
	v_and_or_b32 v13, v21, s33, v23
	global_store_dwordx4 v[14:15], v[6:9], off
	global_store_dwordx4 v[14:15], v[10:13], off offset:256
	s_nop 0
	s_mov_b64 s[16:17], -1
	v_add_co_u32_e32 v10, vcc, s11, v2
	s_waitcnt vmcnt(14)
	v_mul_f32_e32 v2, 0x3c800000, v184
	v_pk_mul_f32 v[4:5], v[48:49], v[2:3] op_sel_hi:[1,0]
	v_pk_mul_f32 v[6:7], v[46:47], v[2:3] op_sel_hi:[1,0]
	v_pk_mul_f32 v[8:9], v[44:45], v[2:3] op_sel_hi:[1,0]
	v_pk_mul_f32 v[12:13], v[42:43], v[2:3] op_sel_hi:[1,0]
	v_addc_co_u32_e32 v11, vcc, 0, v3, vcc
	v_pk_mul_f32 v[14:15], v[40:41], v[2:3] op_sel_hi:[1,0]
	v_pk_mul_f32 v[16:17], v[38:39], v[2:3] op_sel_hi:[1,0]
	v_pk_mul_f32 v[18:19], v[36:37], v[2:3] op_sel_hi:[1,0]
	v_pk_mul_f32 v[2:3], v[34:35], v[2:3] op_sel_hi:[1,0]
	v_bfe_u32 v1, v6, 16, 1
	v_bfe_u32 v20, v7, 16, 1
	v_bfe_u32 v21, v4, 16, 1
	v_bfe_u32 v23, v12, 16, 1
	v_bfe_u32 v25, v8, 16, 1
	v_bfe_u32 v22, v5, 16, 1
	v_bfe_u32 v24, v13, 16, 1
	v_bfe_u32 v26, v9, 16, 1
	v_bfe_u32 v27, v16, 16, 1
	v_bfe_u32 v28, v17, 16, 1
	v_bfe_u32 v29, v14, 16, 1
	v_bfe_u32 v31, v2, 16, 1
	v_bfe_u32 v32, v3, 16, 1
	v_bfe_u32 v33, v18, 16, 1
	v_add3_u32 v1, v6, v1, s37
	v_add3_u32 v6, v7, v20, s37
	v_add3_u32 v4, v4, v21, s37
	v_add3_u32 v7, v12, v23, s37
	v_add3_u32 v8, v8, v25, s37
	v_bfe_u32 v30, v15, 16, 1
	v_bfe_u32 v34, v19, 16, 1
	v_add3_u32 v5, v5, v22, s37
	v_add3_u32 v12, v13, v24, s37
	v_add3_u32 v9, v9, v26, s37
	v_add3_u32 v13, v16, v27, s37
	v_add3_u32 v16, v17, v28, s37
	v_add3_u32 v14, v14, v29, s37
	v_add3_u32 v2, v2, v31, s37
	v_add3_u32 v17, v3, v32, s37
	v_add3_u32 v3, v18, v33, s37
	v_lshrrev_b32_e32 v1, 16, v1
	v_lshrrev_b32_e32 v4, 16, v4
	v_lshrrev_b32_e32 v7, 16, v7
	v_lshrrev_b32_e32 v8, 16, v8
	s_and_b64 vcc, exec, s[38:39]
	v_add3_u32 v15, v15, v30, s37
	v_add3_u32 v18, v19, v34, s37
	v_lshrrev_b32_e32 v13, 16, v13
	v_lshrrev_b32_e32 v14, 16, v14
	v_lshrrev_b32_e32 v19, 16, v2
	v_lshrrev_b32_e32 v20, 16, v3
	v_and_or_b32 v2, v6, s33, v1
	v_and_or_b32 v3, v5, s33, v4
	v_and_or_b32 v4, v12, s33, v7
	v_and_or_b32 v5, v9, s33, v8
	v_and_or_b32 v6, v16, s33, v13
	v_and_or_b32 v7, v15, s33, v14
	v_and_or_b32 v8, v17, s33, v19
	v_and_or_b32 v9, v18, s33, v20
	global_store_dwordx4 v[10:11], v[2:5], off
	global_store_dwordx4 v[10:11], v[6:9], off offset:256
	s_cbranch_vccnz .LBB0_2656
	s_andn2_b64 vcc, exec, s[4:5]
	s_cbranch_vccnz .LBB0_2655
	s_barrier
	s_branch .LBB0_2655
